# GLA pre-pass: the 32 ln(1+e) per item use v_log_f32 * ln2 directly (238 instructions of never-taken denormal scaling / extended-precision multiply removed); on top of attention + combine rewrites
# speedup vs baseline: 1.0058x; 1.0058x over previous
.LBB0_411:
	s_waitcnt vmcnt(14)
	v_readlane_b32 s40, v70, 0
	v_readlane_b32 s41, v71, 0
	s_lshl_b32 s2, s40, 16
	s_and_b32 s40, s40, 0xffff0000
	v_pk_mul_f32 v[74:75], v[4:5], s[40:41] op_sel_hi:[1,0]
	v_pk_mul_f32 v[76:77], v[2:3], s[40:41] op_sel_hi:[1,0]
	s_and_b32 s40, s41, 0xffff0000
	v_readlane_b32 s58, v72, 0
	v_pk_fma_f32 v[74:75], v[28:29], s[2:3], v[74:75] op_sel_hi:[1,0,1]
	v_pk_fma_f32 v[76:77], v[26:27], s[2:3], v[76:77] op_sel_hi:[1,0,1]
	s_lshl_b32 s2, s41, 16
	v_pk_mul_f32 v[80:81], v[10:11], s[40:41] op_sel_hi:[1,0]
	v_pk_add_f32 v[76:77], v[66:67], v[76:77]
	v_pk_mul_f32 v[78:79], v[12:13], s[40:41] op_sel_hi:[1,0]
	v_pk_fma_f32 v[80:81], v[6:7], s[2:3], v[80:81] op_sel_hi:[1,0,1]
	s_and_b32 s40, s58, 0xffff0000
	v_readlane_b32 s66, v73, 0
	v_pk_add_f32 v[74:75], v[68:69], v[74:75]
	v_pk_fma_f32 v[78:79], v[8:9], s[2:3], v[78:79] op_sel_hi:[1,0,1]
	v_pk_add_f32 v[76:77], v[76:77], v[80:81]
	s_lshl_b32 s2, s58, 16
	v_pk_mul_f32 v[80:81], v[18:19], s[40:41] op_sel_hi:[1,0]
	v_pk_add_f32 v[74:75], v[74:75], v[78:79]
	v_pk_mul_f32 v[78:79], v[20:21], s[40:41] op_sel_hi:[1,0]
	v_pk_fma_f32 v[80:81], v[14:15], s[2:3], v[80:81] op_sel_hi:[1,0,1]
	s_and_b32 s40, s66, 0xffff0000
	v_readlane_b32 s67, v70, 1
	v_pk_fma_f32 v[78:79], v[16:17], s[2:3], v[78:79] op_sel_hi:[1,0,1]
	v_pk_add_f32 v[76:77], v[76:77], v[80:81]
	s_lshl_b32 s2, s66, 16
	v_pk_mul_f32 v[80:81], v[30:31], s[40:41] op_sel_hi:[1,0]
	v_pk_add_f32 v[74:75], v[74:75], v[78:79]
	v_pk_mul_f32 v[78:79], v[32:33], s[40:41] op_sel_hi:[1,0]
	v_pk_fma_f32 v[80:81], v[22:23], s[2:3], v[80:81] op_sel_hi:[1,0,1]
	s_and_b32 s40, s67, 0xffff0000
	v_readlane_b32 s73, v71, 1
	v_pk_fma_f32 v[78:79], v[24:25], s[2:3], v[78:79] op_sel_hi:[1,0,1]
	v_pk_add_f32 v[76:77], v[76:77], v[80:81]
	s_lshl_b32 s2, s67, 16
	v_pk_mul_f32 v[80:81], v[38:39], s[40:41] op_sel_hi:[1,0]
	v_pk_add_f32 v[74:75], v[74:75], v[78:79]
	v_pk_mul_f32 v[78:79], v[40:41], s[40:41] op_sel_hi:[1,0]
	v_pk_fma_f32 v[80:81], v[34:35], s[2:3], v[80:81] op_sel_hi:[1,0,1]
	s_and_b32 s40, s73, 0xffff0000
	v_readlane_b32 s74, v72, 1
	v_pk_fma_f32 v[78:79], v[36:37], s[2:3], v[78:79] op_sel_hi:[1,0,1]
	v_pk_add_f32 v[76:77], v[76:77], v[80:81]
	s_lshl_b32 s2, s73, 16
	v_pk_mul_f32 v[80:81], v[46:47], s[40:41] op_sel_hi:[1,0]
	v_pk_add_f32 v[74:75], v[74:75], v[78:79]
	v_pk_mul_f32 v[78:79], v[48:49], s[40:41] op_sel_hi:[1,0]
	v_pk_fma_f32 v[80:81], v[42:43], s[2:3], v[80:81] op_sel_hi:[1,0,1]
	s_and_b32 s40, s74, 0xffff0000
	v_readlane_b32 s75, v73, 1
	v_pk_fma_f32 v[78:79], v[44:45], s[2:3], v[78:79] op_sel_hi:[1,0,1]
	v_pk_add_f32 v[76:77], v[76:77], v[80:81]
	s_lshl_b32 s2, s74, 16
	v_pk_mul_f32 v[80:81], v[54:55], s[40:41] op_sel_hi:[1,0]
	s_and_b32 s58, s75, 0xffff0000
	v_pk_fma_f32 v[80:81], v[50:51], s[2:3], v[80:81] op_sel_hi:[1,0,1]
	v_pk_add_f32 v[74:75], v[74:75], v[78:79]
	v_pk_mul_f32 v[78:79], v[56:57], s[40:41] op_sel_hi:[1,0]
	v_pk_add_f32 v[76:77], v[76:77], v[80:81]
	s_lshl_b32 s40, s75, 16
	v_pk_mul_f32 v[80:81], v[62:63], s[58:59] op_sel_hi:[1,0]
	v_pk_fma_f32 v[78:79], v[52:53], s[2:3], v[78:79] op_sel_hi:[1,0,1]
	v_pk_fma_f32 v[80:81], v[58:59], s[40:41], v[80:81] op_sel_hi:[1,0,1]
	v_pk_add_f32 v[74:75], v[74:75], v[78:79]
	v_pk_add_f32 v[76:77], v[76:77], v[80:81]
	v_pk_mul_f32 v[78:79], v[64:65], s[58:59] op_sel_hi:[1,0]
	v_mul_f32_e64 v80, |v76|, s53
	v_exp_f32_e32 v80, v80
	v_pk_fma_f32 v[78:79], v[60:61], s[40:41], v[78:79] op_sel_hi:[1,0,1]
	v_readlane_b32 s58, v72, 2
	v_pk_add_f32 v[78:79], v[74:75], v[78:79]
	v_add_f32_e32 v80, 1.0, v80
	v_min_f32_e32 v74, 0, v76
	v_mul_f32_e64 v76, |v77|, s53
	v_log_f32_e32 v80, v80
	v_exp_f32_e32 v76, v76
	v_readlane_b32 s66, v73, 2
	v_readlane_b32 s67, v70, 3
	v_mul_f32_e32 v75, 0x3f317217, v80
	v_readlane_b32 s73, v71, 3
	v_readlane_b32 s74, v72, 3
	v_mov_b32_e32 v80, 0
	v_sub_f32_e32 v75, v75, v80
	v_sub_f32_e32 v74, v74, v75
	v_add_f32_e32 v75, 1.0, v76
	v_readlane_b32 s75, v73, 3
	v_mul_f32_e32 v74, 0x3d800000, v74
	v_log_f32_e32 v75, v75
	v_min_f32_e32 v76, 0, v77
	v_mov_b32_e32 v80, 0
	v_max_f32_e32 v74, -1.0, v74
	v_mul_f32_e32 v77, 0x3f317217, v75
	v_and_b32_e32 v196, 0xffff0000, v105
	s_nop 0
	v_mov_b32_e32 v75, v77
	v_mul_f32_e64 v77, |v78|, s53
	v_exp_f32_e32 v77, v77
	v_sub_f32_e32 v75, v75, v80
	v_sub_f32_e32 v75, v76, v75
	v_mul_f32_e32 v75, 0x3d800000, v75
	v_add_f32_e32 v76, 1.0, v77
	v_max_f32_e32 v75, -1.0, v75
	s_nop 0
	v_log_f32_e32 v76, v76
	v_min_f32_e32 v77, 0, v78
	v_mov_b32_e32 v80, 0
	v_mul_f32_e32 v78, 0x3f317217, v76
	s_nop 1
	v_mov_b32_e32 v76, v78
	v_mul_f32_e64 v78, |v79|, s53
	v_exp_f32_e32 v78, v78
	v_sub_f32_e32 v76, v76, v80
	v_sub_f32_e32 v76, v77, v76
	v_mul_f32_e32 v76, 0x3d800000, v76
	v_add_f32_e32 v77, 1.0, v78
	v_max_f32_e32 v76, -1.0, v76
	s_nop 0
	v_log_f32_e32 v77, v77
	v_min_f32_e32 v78, 0, v79
	v_mul_f32_e32 v79, 0x3f317217, v77
	s_nop 1
	v_mov_b32_e32 v77, v79
	v_mov_b32_e32 v79, 0
	v_readlane_b32 s40, v70, 2
	v_sub_f32_e32 v77, v77, v79
	v_readlane_b32 s41, v71, 2
	s_lshl_b32 s2, s40, 16
	s_and_b32 s40, s40, 0xffff0000
	v_sub_f32_e32 v77, v78, v77
	v_pk_mul_f32 v[78:79], v[4:5], s[40:41] op_sel_hi:[1,0]
	v_pk_mul_f32 v[80:81], v[2:3], s[40:41] op_sel_hi:[1,0]
	s_and_b32 s40, s41, 0xffff0000
	v_pk_fma_f32 v[78:79], v[28:29], s[2:3], v[78:79] op_sel_hi:[1,0,1]
	v_pk_fma_f32 v[80:81], v[26:27], s[2:3], v[80:81] op_sel_hi:[1,0,1]
	s_lshl_b32 s2, s41, 16
	v_pk_mul_f32 v[152:153], v[10:11], s[40:41] op_sel_hi:[1,0]
	v_pk_add_f32 v[80:81], v[66:67], v[80:81]
	v_pk_mul_f32 v[150:151], v[12:13], s[40:41] op_sel_hi:[1,0]
	v_pk_fma_f32 v[152:153], v[6:7], s[2:3], v[152:153] op_sel_hi:[1,0,1]
	s_and_b32 s40, s58, 0xffff0000
	v_pk_add_f32 v[78:79], v[68:69], v[78:79]
	v_pk_fma_f32 v[150:151], v[8:9], s[2:3], v[150:151] op_sel_hi:[1,0,1]
	v_pk_add_f32 v[80:81], v[80:81], v[152:153]
	s_lshl_b32 s2, s58, 16
	v_pk_mul_f32 v[152:153], v[18:19], s[40:41] op_sel_hi:[1,0]
	v_pk_add_f32 v[78:79], v[78:79], v[150:151]
	v_pk_mul_f32 v[150:151], v[20:21], s[40:41] op_sel_hi:[1,0]
	v_pk_fma_f32 v[152:153], v[14:15], s[2:3], v[152:153] op_sel_hi:[1,0,1]
	s_and_b32 s40, s66, 0xffff0000
	v_pk_fma_f32 v[150:151], v[16:17], s[2:3], v[150:151] op_sel_hi:[1,0,1]
	v_pk_add_f32 v[80:81], v[80:81], v[152:153]
	s_lshl_b32 s2, s66, 16
	v_pk_mul_f32 v[152:153], v[30:31], s[40:41] op_sel_hi:[1,0]
	v_pk_add_f32 v[78:79], v[78:79], v[150:151]
	v_pk_mul_f32 v[150:151], v[32:33], s[40:41] op_sel_hi:[1,0]
	v_pk_fma_f32 v[152:153], v[22:23], s[2:3], v[152:153] op_sel_hi:[1,0,1]
	s_and_b32 s40, s67, 0xffff0000
	v_pk_fma_f32 v[150:151], v[24:25], s[2:3], v[150:151] op_sel_hi:[1,0,1]
	v_pk_add_f32 v[80:81], v[80:81], v[152:153]
	s_lshl_b32 s2, s67, 16
	v_pk_mul_f32 v[152:153], v[38:39], s[40:41] op_sel_hi:[1,0]
	v_pk_add_f32 v[78:79], v[78:79], v[150:151]
	v_pk_mul_f32 v[150:151], v[40:41], s[40:41] op_sel_hi:[1,0]
	v_pk_fma_f32 v[152:153], v[34:35], s[2:3], v[152:153] op_sel_hi:[1,0,1]
	s_and_b32 s40, s73, 0xffff0000
	v_pk_fma_f32 v[150:151], v[36:37], s[2:3], v[150:151] op_sel_hi:[1,0,1]
	v_pk_add_f32 v[80:81], v[80:81], v[152:153]
	s_lshl_b32 s2, s73, 16
	v_pk_mul_f32 v[152:153], v[46:47], s[40:41] op_sel_hi:[1,0]
	v_pk_add_f32 v[78:79], v[78:79], v[150:151]
	v_pk_mul_f32 v[150:151], v[48:49], s[40:41] op_sel_hi:[1,0]
	v_pk_fma_f32 v[152:153], v[42:43], s[2:3], v[152:153] op_sel_hi:[1,0,1]
	s_and_b32 s40, s74, 0xffff0000
	v_pk_fma_f32 v[150:151], v[44:45], s[2:3], v[150:151] op_sel_hi:[1,0,1]
	v_pk_add_f32 v[80:81], v[80:81], v[152:153]
	s_lshl_b32 s2, s74, 16
	v_pk_mul_f32 v[152:153], v[54:55], s[40:41] op_sel_hi:[1,0]
	s_and_b32 s58, s75, 0xffff0000
	v_pk_fma_f32 v[152:153], v[50:51], s[2:3], v[152:153] op_sel_hi:[1,0,1]
	v_pk_add_f32 v[78:79], v[78:79], v[150:151]
	v_pk_mul_f32 v[150:151], v[56:57], s[40:41] op_sel_hi:[1,0]
	v_pk_add_f32 v[80:81], v[80:81], v[152:153]
	s_lshl_b32 s40, s75, 16
	v_pk_mul_f32 v[152:153], v[62:63], s[58:59] op_sel_hi:[1,0]
	v_pk_fma_f32 v[150:151], v[52:53], s[2:3], v[150:151] op_sel_hi:[1,0,1]
	v_pk_fma_f32 v[152:153], v[58:59], s[40:41], v[152:153] op_sel_hi:[1,0,1]
	v_pk_add_f32 v[78:79], v[78:79], v[150:151]
	v_pk_add_f32 v[80:81], v[80:81], v[152:153]
	v_pk_mul_f32 v[150:151], v[64:65], s[58:59] op_sel_hi:[1,0]
	v_mul_f32_e64 v152, |v80|, s53
	v_exp_f32_e32 v152, v152
	v_pk_fma_f32 v[150:151], v[60:61], s[40:41], v[150:151] op_sel_hi:[1,0,1]
	v_min_f32_e32 v80, 0, v80
	v_pk_add_f32 v[78:79], v[78:79], v[150:151]
	v_add_f32_e32 v152, 1.0, v152
	v_mul_f32_e64 v151, |v81|, s53
	v_exp_f32_e32 v151, v151
	v_log_f32_e32 v152, v152
	v_min_f32_e32 v81, 0, v81
	v_readlane_b32 s58, v72, 4
	v_readlane_b32 s66, v73, 4
	v_mul_f32_e32 v150, 0x3f317217, v152
	v_readlane_b32 s67, v70, 5
	v_readlane_b32 s73, v71, 5
	v_mov_b32_e32 v152, 0
	v_sub_f32_e32 v150, v150, v152
	v_sub_f32_e32 v80, v80, v150
	v_add_f32_e32 v150, 1.0, v151
	v_readlane_b32 s74, v72, 5
	v_readlane_b32 s75, v73, 5
	v_log_f32_e32 v150, v150
	v_mov_b32_e32 v152, 0
	v_mul_f32_e32 v80, 0x3d800000, v80
	v_max_f32_e32 v80, -1.0, v80
	v_mul_f32_e32 v151, 0x3f317217, v150
	v_mul_f32_e32 v77, 0x3d800000, v77
	v_max_f32_e32 v77, -1.0, v77
	v_mov_b32_e32 v150, v151
	v_mul_f32_e64 v151, |v78|, s53
	v_exp_f32_e32 v151, v151
	v_sub_f32_e32 v150, v150, v152
	v_sub_f32_e32 v81, v81, v150
	v_min_f32_e32 v78, 0, v78
	v_add_f32_e32 v150, 1.0, v151
	v_mul_f32_e32 v81, 0x3d800000, v81
	v_max_f32_e32 v81, -1.0, v81
	v_log_f32_e32 v150, v150
	v_mov_b32_e32 v152, 0
	v_pk_add_f32 v[190:191], v[76:77], 0 op_sel_hi:[1,0]
	v_mul_f32_e32 v151, 0x3f317217, v150
	s_nop 1
	v_mov_b32_e32 v150, v151
	v_mul_f32_e64 v151, |v79|, s53
	v_exp_f32_e32 v151, v151
	v_sub_f32_e32 v150, v150, v152
	v_sub_f32_e32 v78, v78, v150
	v_min_f32_e32 v79, 0, v79
	v_add_f32_e32 v150, 1.0, v151
	v_mul_f32_e32 v78, 0x3d800000, v78
	v_max_f32_e32 v78, -1.0, v78
	v_log_f32_e32 v150, v150
	s_nop 0
	v_mul_f32_e32 v151, 0x3f317217, v150
	s_nop 1
	v_mov_b32_e32 v150, v151
	v_mov_b32_e32 v151, 0
	v_readlane_b32 s40, v70, 4
	v_sub_f32_e32 v150, v150, v151
	v_readlane_b32 s41, v71, 4
	s_lshl_b32 s2, s40, 16
	s_and_b32 s40, s40, 0xffff0000
	v_sub_f32_e32 v79, v79, v150
	v_pk_mul_f32 v[150:151], v[4:5], s[40:41] op_sel_hi:[1,0]
	v_pk_mul_f32 v[152:153], v[2:3], s[40:41] op_sel_hi:[1,0]
	s_and_b32 s40, s41, 0xffff0000
	v_pk_fma_f32 v[150:151], v[28:29], s[2:3], v[150:151] op_sel_hi:[1,0,1]
	v_pk_fma_f32 v[152:153], v[26:27], s[2:3], v[152:153] op_sel_hi:[1,0,1]
	s_lshl_b32 s2, s41, 16
	v_pk_mul_f32 v[156:157], v[10:11], s[40:41] op_sel_hi:[1,0]
	v_pk_add_f32 v[152:153], v[66:67], v[152:153]
	v_pk_mul_f32 v[154:155], v[12:13], s[40:41] op_sel_hi:[1,0]
	v_pk_fma_f32 v[156:157], v[6:7], s[2:3], v[156:157] op_sel_hi:[1,0,1]
	s_and_b32 s40, s58, 0xffff0000
	v_pk_add_f32 v[150:151], v[68:69], v[150:151]
	v_pk_fma_f32 v[154:155], v[8:9], s[2:3], v[154:155] op_sel_hi:[1,0,1]
	v_pk_add_f32 v[152:153], v[152:153], v[156:157]
	s_lshl_b32 s2, s58, 16
	v_pk_mul_f32 v[156:157], v[18:19], s[40:41] op_sel_hi:[1,0]
	v_pk_add_f32 v[150:151], v[150:151], v[154:155]
	v_pk_mul_f32 v[154:155], v[20:21], s[40:41] op_sel_hi:[1,0]
	v_pk_fma_f32 v[156:157], v[14:15], s[2:3], v[156:157] op_sel_hi:[1,0,1]
	s_and_b32 s40, s66, 0xffff0000
	v_pk_fma_f32 v[154:155], v[16:17], s[2:3], v[154:155] op_sel_hi:[1,0,1]
	v_pk_add_f32 v[152:153], v[152:153], v[156:157]
	s_lshl_b32 s2, s66, 16
	v_pk_mul_f32 v[156:157], v[30:31], s[40:41] op_sel_hi:[1,0]
	v_pk_add_f32 v[150:151], v[150:151], v[154:155]
	v_pk_mul_f32 v[154:155], v[32:33], s[40:41] op_sel_hi:[1,0]
	v_pk_fma_f32 v[156:157], v[22:23], s[2:3], v[156:157] op_sel_hi:[1,0,1]
	s_and_b32 s40, s67, 0xffff0000
	v_pk_fma_f32 v[154:155], v[24:25], s[2:3], v[154:155] op_sel_hi:[1,0,1]
	v_pk_add_f32 v[152:153], v[152:153], v[156:157]
	s_lshl_b32 s2, s67, 16
	v_pk_mul_f32 v[156:157], v[38:39], s[40:41] op_sel_hi:[1,0]
	v_pk_add_f32 v[150:151], v[150:151], v[154:155]
	v_pk_mul_f32 v[154:155], v[40:41], s[40:41] op_sel_hi:[1,0]
	v_pk_fma_f32 v[156:157], v[34:35], s[2:3], v[156:157] op_sel_hi:[1,0,1]
	s_and_b32 s40, s73, 0xffff0000
	v_pk_fma_f32 v[154:155], v[36:37], s[2:3], v[154:155] op_sel_hi:[1,0,1]
	v_pk_add_f32 v[152:153], v[152:153], v[156:157]
	s_lshl_b32 s2, s73, 16
	v_pk_mul_f32 v[156:157], v[46:47], s[40:41] op_sel_hi:[1,0]
	v_pk_add_f32 v[150:151], v[150:151], v[154:155]
	v_pk_mul_f32 v[154:155], v[48:49], s[40:41] op_sel_hi:[1,0]
	v_pk_fma_f32 v[156:157], v[42:43], s[2:3], v[156:157] op_sel_hi:[1,0,1]
	s_and_b32 s40, s74, 0xffff0000
	v_pk_fma_f32 v[154:155], v[44:45], s[2:3], v[154:155] op_sel_hi:[1,0,1]
	v_pk_add_f32 v[152:153], v[152:153], v[156:157]
	s_lshl_b32 s2, s74, 16
	v_pk_mul_f32 v[156:157], v[54:55], s[40:41] op_sel_hi:[1,0]
	s_and_b32 s58, s75, 0xffff0000
	v_pk_fma_f32 v[156:157], v[50:51], s[2:3], v[156:157] op_sel_hi:[1,0,1]
	v_pk_add_f32 v[150:151], v[150:151], v[154:155]
	v_pk_mul_f32 v[154:155], v[56:57], s[40:41] op_sel_hi:[1,0]
	v_pk_add_f32 v[152:153], v[152:153], v[156:157]
	s_lshl_b32 s40, s75, 16
	v_pk_mul_f32 v[156:157], v[62:63], s[58:59] op_sel_hi:[1,0]
	v_pk_fma_f32 v[154:155], v[52:53], s[2:3], v[154:155] op_sel_hi:[1,0,1]
	v_pk_fma_f32 v[156:157], v[58:59], s[40:41], v[156:157] op_sel_hi:[1,0,1]
	v_pk_add_f32 v[150:151], v[150:151], v[154:155]
	v_pk_add_f32 v[152:153], v[152:153], v[156:157]
	v_pk_mul_f32 v[154:155], v[64:65], s[58:59] op_sel_hi:[1,0]
	v_mul_f32_e64 v156, |v152|, s53
	v_exp_f32_e32 v156, v156
	v_pk_fma_f32 v[154:155], v[60:61], s[40:41], v[154:155] op_sel_hi:[1,0,1]
	v_min_f32_e32 v152, 0, v152
	v_pk_add_f32 v[150:151], v[150:151], v[154:155]
	v_add_f32_e32 v156, 1.0, v156
	v_mul_f32_e64 v155, |v153|, s53
	v_exp_f32_e32 v155, v155
	v_log_f32_e32 v156, v156
	v_min_f32_e32 v153, 0, v153
	v_readlane_b32 s58, v72, 6
	v_readlane_b32 s66, v73, 6
	v_mul_f32_e32 v154, 0x3f317217, v156
	v_readlane_b32 s67, v70, 7
	v_readlane_b32 s73, v71, 7
	v_mov_b32_e32 v156, 0
	v_sub_f32_e32 v154, v154, v156
	v_sub_f32_e32 v152, v152, v154
	v_add_f32_e32 v154, 1.0, v155
	v_readlane_b32 s74, v72, 7
	v_readlane_b32 s75, v73, 7
	v_log_f32_e32 v154, v154
	v_mov_b32_e32 v156, 0
	v_mul_f32_e32 v152, 0x3d800000, v152
	v_max_f32_e32 v152, -1.0, v152
	v_mul_f32_e32 v155, 0x3f317217, v154
	v_mul_f32_e32 v79, 0x3d800000, v79
	v_max_f32_e32 v79, -1.0, v79
	v_mov_b32_e32 v154, v155
	v_mul_f32_e64 v155, |v150|, s53
	v_exp_f32_e32 v155, v155
	v_sub_f32_e32 v154, v154, v156
	v_sub_f32_e32 v153, v153, v154
	v_min_f32_e32 v150, 0, v150
	v_add_f32_e32 v154, 1.0, v155
	v_mul_f32_e32 v153, 0x3d800000, v153
	v_max_f32_e32 v153, -1.0, v153
	v_log_f32_e32 v154, v154
	v_mov_b32_e32 v156, 0
	v_mul_f32_e32 v155, 0x3f317217, v154
	s_nop 1
	v_mov_b32_e32 v154, v155
	v_mul_f32_e64 v155, |v151|, s53
	v_exp_f32_e32 v155, v155
	v_sub_f32_e32 v154, v154, v156
	v_sub_f32_e32 v150, v150, v154
	v_min_f32_e32 v151, 0, v151
	v_add_f32_e32 v154, 1.0, v155
	v_mul_f32_e32 v150, 0x3d800000, v150
	v_max_f32_e32 v150, -1.0, v150
	v_log_f32_e32 v154, v154
	s_nop 0
	v_mul_f32_e32 v155, 0x3f317217, v154
	s_nop 1
	v_mov_b32_e32 v154, v155
	v_mov_b32_e32 v155, 0
	v_readlane_b32 s40, v70, 6
	v_sub_f32_e32 v154, v154, v155
	v_readlane_b32 s41, v71, 6
	s_lshl_b32 s2, s40, 16
	s_and_b32 s40, s40, 0xffff0000
	v_sub_f32_e32 v151, v151, v154
	v_pk_mul_f32 v[154:155], v[4:5], s[40:41] op_sel_hi:[1,0]
	v_pk_mul_f32 v[156:157], v[2:3], s[40:41] op_sel_hi:[1,0]
	s_and_b32 s40, s41, 0xffff0000
	v_pk_fma_f32 v[154:155], v[28:29], s[2:3], v[154:155] op_sel_hi:[1,0,1]
	v_pk_fma_f32 v[156:157], v[26:27], s[2:3], v[156:157] op_sel_hi:[1,0,1]
	s_lshl_b32 s2, s41, 16
	v_pk_mul_f32 v[160:161], v[10:11], s[40:41] op_sel_hi:[1,0]
	v_pk_add_f32 v[156:157], v[66:67], v[156:157]
	v_pk_mul_f32 v[158:159], v[12:13], s[40:41] op_sel_hi:[1,0]
	v_pk_fma_f32 v[160:161], v[6:7], s[2:3], v[160:161] op_sel_hi:[1,0,1]
	s_and_b32 s40, s58, 0xffff0000
	v_pk_add_f32 v[154:155], v[68:69], v[154:155]
	v_pk_fma_f32 v[158:159], v[8:9], s[2:3], v[158:159] op_sel_hi:[1,0,1]
	v_pk_add_f32 v[156:157], v[156:157], v[160:161]
	s_lshl_b32 s2, s58, 16
	v_pk_mul_f32 v[160:161], v[18:19], s[40:41] op_sel_hi:[1,0]
	v_pk_add_f32 v[154:155], v[154:155], v[158:159]
	v_pk_mul_f32 v[158:159], v[20:21], s[40:41] op_sel_hi:[1,0]
	v_pk_fma_f32 v[160:161], v[14:15], s[2:3], v[160:161] op_sel_hi:[1,0,1]
	s_and_b32 s40, s66, 0xffff0000
	v_pk_fma_f32 v[158:159], v[16:17], s[2:3], v[158:159] op_sel_hi:[1,0,1]
	v_pk_add_f32 v[156:157], v[156:157], v[160:161]
	s_lshl_b32 s2, s66, 16
	v_pk_mul_f32 v[160:161], v[30:31], s[40:41] op_sel_hi:[1,0]
	v_pk_add_f32 v[154:155], v[154:155], v[158:159]
	v_pk_mul_f32 v[158:159], v[32:33], s[40:41] op_sel_hi:[1,0]
	v_pk_fma_f32 v[160:161], v[22:23], s[2:3], v[160:161] op_sel_hi:[1,0,1]
	s_and_b32 s40, s67, 0xffff0000
	v_pk_fma_f32 v[158:159], v[24:25], s[2:3], v[158:159] op_sel_hi:[1,0,1]
	v_pk_add_f32 v[156:157], v[156:157], v[160:161]
	s_lshl_b32 s2, s67, 16
	v_pk_mul_f32 v[160:161], v[38:39], s[40:41] op_sel_hi:[1,0]
	v_pk_add_f32 v[154:155], v[154:155], v[158:159]
	v_pk_mul_f32 v[158:159], v[40:41], s[40:41] op_sel_hi:[1,0]
	v_pk_fma_f32 v[160:161], v[34:35], s[2:3], v[160:161] op_sel_hi:[1,0,1]
	s_and_b32 s40, s73, 0xffff0000
	v_pk_fma_f32 v[158:159], v[36:37], s[2:3], v[158:159] op_sel_hi:[1,0,1]
	v_pk_add_f32 v[156:157], v[156:157], v[160:161]
	s_lshl_b32 s2, s73, 16
	v_pk_mul_f32 v[160:161], v[46:47], s[40:41] op_sel_hi:[1,0]
	v_pk_add_f32 v[154:155], v[154:155], v[158:159]
	v_pk_mul_f32 v[158:159], v[48:49], s[40:41] op_sel_hi:[1,0]
	v_pk_fma_f32 v[160:161], v[42:43], s[2:3], v[160:161] op_sel_hi:[1,0,1]
	s_and_b32 s40, s74, 0xffff0000
	v_pk_fma_f32 v[158:159], v[44:45], s[2:3], v[158:159] op_sel_hi:[1,0,1]
	v_pk_add_f32 v[156:157], v[156:157], v[160:161]
	s_lshl_b32 s2, s74, 16
	v_pk_mul_f32 v[160:161], v[54:55], s[40:41] op_sel_hi:[1,0]
	s_and_b32 s58, s75, 0xffff0000
	v_pk_fma_f32 v[160:161], v[50:51], s[2:3], v[160:161] op_sel_hi:[1,0,1]
	v_pk_add_f32 v[154:155], v[154:155], v[158:159]
	v_pk_mul_f32 v[158:159], v[56:57], s[40:41] op_sel_hi:[1,0]
	v_pk_add_f32 v[156:157], v[156:157], v[160:161]
	s_lshl_b32 s40, s75, 16
	v_pk_mul_f32 v[160:161], v[62:63], s[58:59] op_sel_hi:[1,0]
	v_pk_fma_f32 v[158:159], v[52:53], s[2:3], v[158:159] op_sel_hi:[1,0,1]
	v_pk_fma_f32 v[160:161], v[58:59], s[40:41], v[160:161] op_sel_hi:[1,0,1]
	v_pk_add_f32 v[154:155], v[154:155], v[158:159]
	v_pk_add_f32 v[156:157], v[156:157], v[160:161]
	v_pk_mul_f32 v[158:159], v[64:65], s[58:59] op_sel_hi:[1,0]
	v_mul_f32_e64 v160, |v156|, s53
	v_exp_f32_e32 v160, v160
	v_pk_fma_f32 v[158:159], v[60:61], s[40:41], v[158:159] op_sel_hi:[1,0,1]
	v_min_f32_e32 v156, 0, v156
	v_pk_add_f32 v[154:155], v[154:155], v[158:159]
	v_add_f32_e32 v160, 1.0, v160
	v_mul_f32_e64 v159, |v157|, s53
	v_exp_f32_e32 v159, v159
	v_log_f32_e32 v160, v160
	v_min_f32_e32 v157, 0, v157
	v_readlane_b32 s58, v72, 8
	v_readlane_b32 s66, v73, 8
	v_mul_f32_e32 v158, 0x3f317217, v160
	v_readlane_b32 s67, v70, 9
	v_readlane_b32 s73, v71, 9
	v_mov_b32_e32 v160, 0
	v_sub_f32_e32 v158, v158, v160
	v_sub_f32_e32 v156, v156, v158
	v_add_f32_e32 v158, 1.0, v159
	v_readlane_b32 s74, v72, 9
	v_readlane_b32 s75, v73, 9
	v_log_f32_e32 v158, v158
	v_mov_b32_e32 v160, 0
	v_mul_f32_e32 v156, 0x3d800000, v156
	v_max_f32_e32 v156, -1.0, v156
	v_mul_f32_e32 v159, 0x3f317217, v158
	v_mul_f32_e32 v151, 0x3d800000, v151
	v_max_f32_e32 v151, -1.0, v151
	v_mov_b32_e32 v158, v159
	v_mul_f32_e64 v159, |v154|, s53
	v_exp_f32_e32 v159, v159
	v_sub_f32_e32 v158, v158, v160
	v_sub_f32_e32 v157, v157, v158
	v_min_f32_e32 v154, 0, v154
	v_add_f32_e32 v158, 1.0, v159
	v_mul_f32_e32 v157, 0x3d800000, v157
	v_max_f32_e32 v157, -1.0, v157
	v_log_f32_e32 v158, v158
	v_mov_b32_e32 v160, 0
	v_mul_f32_e32 v159, 0x3f317217, v158
	s_nop 1
	v_mov_b32_e32 v158, v159
	v_mul_f32_e64 v159, |v155|, s53
	v_exp_f32_e32 v159, v159
	v_sub_f32_e32 v158, v158, v160
	v_sub_f32_e32 v154, v154, v158
	v_min_f32_e32 v155, 0, v155
	v_add_f32_e32 v158, 1.0, v159
	v_mul_f32_e32 v154, 0x3d800000, v154
	v_max_f32_e32 v154, -1.0, v154
	v_log_f32_e32 v158, v158
	s_nop 0
	v_mul_f32_e32 v159, 0x3f317217, v158
	s_nop 1
	v_mov_b32_e32 v158, v159
	v_mov_b32_e32 v159, 0
	v_readlane_b32 s40, v70, 8
	v_sub_f32_e32 v158, v158, v159
	v_readlane_b32 s41, v71, 8
	s_lshl_b32 s2, s40, 16
	s_and_b32 s40, s40, 0xffff0000
	v_sub_f32_e32 v155, v155, v158
	v_pk_mul_f32 v[158:159], v[4:5], s[40:41] op_sel_hi:[1,0]
	v_pk_mul_f32 v[160:161], v[2:3], s[40:41] op_sel_hi:[1,0]
	s_and_b32 s40, s41, 0xffff0000
	v_pk_fma_f32 v[158:159], v[28:29], s[2:3], v[158:159] op_sel_hi:[1,0,1]
	v_pk_fma_f32 v[160:161], v[26:27], s[2:3], v[160:161] op_sel_hi:[1,0,1]
	s_lshl_b32 s2, s41, 16
	v_pk_mul_f32 v[164:165], v[10:11], s[40:41] op_sel_hi:[1,0]
	v_pk_add_f32 v[160:161], v[66:67], v[160:161]
	v_pk_mul_f32 v[162:163], v[12:13], s[40:41] op_sel_hi:[1,0]
	v_pk_fma_f32 v[164:165], v[6:7], s[2:3], v[164:165] op_sel_hi:[1,0,1]
	s_and_b32 s40, s58, 0xffff0000
	v_pk_add_f32 v[158:159], v[68:69], v[158:159]
	v_pk_fma_f32 v[162:163], v[8:9], s[2:3], v[162:163] op_sel_hi:[1,0,1]
	v_pk_add_f32 v[160:161], v[160:161], v[164:165]
	s_lshl_b32 s2, s58, 16
	v_pk_mul_f32 v[164:165], v[18:19], s[40:41] op_sel_hi:[1,0]
	v_pk_add_f32 v[158:159], v[158:159], v[162:163]
	v_pk_mul_f32 v[162:163], v[20:21], s[40:41] op_sel_hi:[1,0]
	v_pk_fma_f32 v[164:165], v[14:15], s[2:3], v[164:165] op_sel_hi:[1,0,1]
	s_and_b32 s40, s66, 0xffff0000
	v_pk_fma_f32 v[162:163], v[16:17], s[2:3], v[162:163] op_sel_hi:[1,0,1]
	v_pk_add_f32 v[160:161], v[160:161], v[164:165]
	s_lshl_b32 s2, s66, 16
	v_pk_mul_f32 v[164:165], v[30:31], s[40:41] op_sel_hi:[1,0]
	v_pk_add_f32 v[158:159], v[158:159], v[162:163]
	v_pk_mul_f32 v[162:163], v[32:33], s[40:41] op_sel_hi:[1,0]
	v_pk_fma_f32 v[164:165], v[22:23], s[2:3], v[164:165] op_sel_hi:[1,0,1]
	s_and_b32 s40, s67, 0xffff0000
	v_pk_fma_f32 v[162:163], v[24:25], s[2:3], v[162:163] op_sel_hi:[1,0,1]
	v_pk_add_f32 v[160:161], v[160:161], v[164:165]
	s_lshl_b32 s2, s67, 16
	v_pk_mul_f32 v[164:165], v[38:39], s[40:41] op_sel_hi:[1,0]
	v_pk_add_f32 v[158:159], v[158:159], v[162:163]
	v_pk_mul_f32 v[162:163], v[40:41], s[40:41] op_sel_hi:[1,0]
	v_pk_fma_f32 v[164:165], v[34:35], s[2:3], v[164:165] op_sel_hi:[1,0,1]
	s_and_b32 s40, s73, 0xffff0000
	v_pk_fma_f32 v[162:163], v[36:37], s[2:3], v[162:163] op_sel_hi:[1,0,1]
	v_pk_add_f32 v[160:161], v[160:161], v[164:165]
	s_lshl_b32 s2, s73, 16
	v_pk_mul_f32 v[164:165], v[46:47], s[40:41] op_sel_hi:[1,0]
	v_pk_add_f32 v[158:159], v[158:159], v[162:163]
	v_pk_mul_f32 v[162:163], v[48:49], s[40:41] op_sel_hi:[1,0]
	v_pk_fma_f32 v[164:165], v[42:43], s[2:3], v[164:165] op_sel_hi:[1,0,1]
	s_and_b32 s40, s74, 0xffff0000
	v_pk_fma_f32 v[162:163], v[44:45], s[2:3], v[162:163] op_sel_hi:[1,0,1]
	v_pk_add_f32 v[160:161], v[160:161], v[164:165]
	s_lshl_b32 s2, s74, 16
	v_pk_mul_f32 v[164:165], v[54:55], s[40:41] op_sel_hi:[1,0]
	s_and_b32 s58, s75, 0xffff0000
	v_pk_fma_f32 v[164:165], v[50:51], s[2:3], v[164:165] op_sel_hi:[1,0,1]
	v_pk_add_f32 v[158:159], v[158:159], v[162:163]
	v_pk_mul_f32 v[162:163], v[56:57], s[40:41] op_sel_hi:[1,0]
	v_pk_add_f32 v[160:161], v[160:161], v[164:165]
	s_lshl_b32 s40, s75, 16
	v_pk_mul_f32 v[164:165], v[62:63], s[58:59] op_sel_hi:[1,0]
	v_pk_fma_f32 v[162:163], v[52:53], s[2:3], v[162:163] op_sel_hi:[1,0,1]
	v_pk_fma_f32 v[164:165], v[58:59], s[40:41], v[164:165] op_sel_hi:[1,0,1]
	v_pk_add_f32 v[158:159], v[158:159], v[162:163]
	v_pk_add_f32 v[160:161], v[160:161], v[164:165]
	v_pk_mul_f32 v[162:163], v[64:65], s[58:59] op_sel_hi:[1,0]
	v_mul_f32_e64 v164, |v160|, s53
	v_exp_f32_e32 v164, v164
	v_pk_fma_f32 v[162:163], v[60:61], s[40:41], v[162:163] op_sel_hi:[1,0,1]
	v_min_f32_e32 v160, 0, v160
	v_pk_add_f32 v[158:159], v[158:159], v[162:163]
	v_add_f32_e32 v164, 1.0, v164
	v_mul_f32_e64 v163, |v161|, s53
	v_exp_f32_e32 v163, v163
	v_log_f32_e32 v164, v164
	v_min_f32_e32 v161, 0, v161
	v_readlane_b32 s58, v72, 10
	v_readlane_b32 s66, v73, 10
	v_mul_f32_e32 v162, 0x3f317217, v164
	v_readlane_b32 s67, v70, 11
	v_readlane_b32 s73, v71, 11
	v_mov_b32_e32 v164, 0
	v_sub_f32_e32 v162, v162, v164
	v_sub_f32_e32 v160, v160, v162
	v_add_f32_e32 v162, 1.0, v163
	v_readlane_b32 s74, v72, 11
	v_readlane_b32 s75, v73, 11
	v_log_f32_e32 v162, v162
	v_mov_b32_e32 v164, 0
	v_mul_f32_e32 v160, 0x3d800000, v160
	v_max_f32_e32 v160, -1.0, v160
	v_mul_f32_e32 v163, 0x3f317217, v162
	v_mul_f32_e32 v155, 0x3d800000, v155
	v_max_f32_e32 v155, -1.0, v155
	v_mov_b32_e32 v162, v163
	v_mul_f32_e64 v163, |v158|, s53
	v_exp_f32_e32 v163, v163
	v_sub_f32_e32 v162, v162, v164
	v_sub_f32_e32 v161, v161, v162
	v_min_f32_e32 v158, 0, v158
	v_add_f32_e32 v162, 1.0, v163
	v_mul_f32_e32 v161, 0x3d800000, v161
	v_max_f32_e32 v161, -1.0, v161
	v_log_f32_e32 v162, v162
	v_mov_b32_e32 v164, 0
	v_mul_f32_e32 v163, 0x3f317217, v162
	s_nop 1
	v_mov_b32_e32 v162, v163
	v_mul_f32_e64 v163, |v159|, s53
	v_exp_f32_e32 v163, v163
	v_sub_f32_e32 v162, v162, v164
	v_sub_f32_e32 v158, v158, v162
	v_min_f32_e32 v159, 0, v159
	v_add_f32_e32 v162, 1.0, v163
	v_mul_f32_e32 v158, 0x3d800000, v158
	v_max_f32_e32 v158, -1.0, v158
	v_log_f32_e32 v162, v162
	s_nop 0
	v_mul_f32_e32 v163, 0x3f317217, v162
	s_nop 1
	v_mov_b32_e32 v162, v163
	v_mov_b32_e32 v163, 0
	v_readlane_b32 s40, v70, 10
	v_sub_f32_e32 v162, v162, v163
	v_readlane_b32 s41, v71, 10
	s_lshl_b32 s2, s40, 16
	s_and_b32 s40, s40, 0xffff0000
	v_sub_f32_e32 v159, v159, v162
	v_pk_mul_f32 v[162:163], v[4:5], s[40:41] op_sel_hi:[1,0]
	v_pk_mul_f32 v[164:165], v[2:3], s[40:41] op_sel_hi:[1,0]
	s_and_b32 s40, s41, 0xffff0000
	v_pk_fma_f32 v[162:163], v[28:29], s[2:3], v[162:163] op_sel_hi:[1,0,1]
	v_pk_fma_f32 v[164:165], v[26:27], s[2:3], v[164:165] op_sel_hi:[1,0,1]
	s_lshl_b32 s2, s41, 16
	v_pk_mul_f32 v[168:169], v[10:11], s[40:41] op_sel_hi:[1,0]
	v_pk_add_f32 v[164:165], v[66:67], v[164:165]
	v_pk_mul_f32 v[166:167], v[12:13], s[40:41] op_sel_hi:[1,0]
	v_pk_fma_f32 v[168:169], v[6:7], s[2:3], v[168:169] op_sel_hi:[1,0,1]
	s_and_b32 s40, s58, 0xffff0000
	v_pk_add_f32 v[162:163], v[68:69], v[162:163]
	v_pk_fma_f32 v[166:167], v[8:9], s[2:3], v[166:167] op_sel_hi:[1,0,1]
	v_pk_add_f32 v[164:165], v[164:165], v[168:169]
	s_lshl_b32 s2, s58, 16
	v_pk_mul_f32 v[168:169], v[18:19], s[40:41] op_sel_hi:[1,0]
	v_pk_add_f32 v[162:163], v[162:163], v[166:167]
	v_pk_mul_f32 v[166:167], v[20:21], s[40:41] op_sel_hi:[1,0]
	v_pk_fma_f32 v[168:169], v[14:15], s[2:3], v[168:169] op_sel_hi:[1,0,1]
	s_and_b32 s40, s66, 0xffff0000
	v_pk_fma_f32 v[166:167], v[16:17], s[2:3], v[166:167] op_sel_hi:[1,0,1]
	v_pk_add_f32 v[164:165], v[164:165], v[168:169]
	s_lshl_b32 s2, s66, 16
	v_pk_mul_f32 v[168:169], v[30:31], s[40:41] op_sel_hi:[1,0]
	v_pk_add_f32 v[162:163], v[162:163], v[166:167]
	v_pk_mul_f32 v[166:167], v[32:33], s[40:41] op_sel_hi:[1,0]
	v_pk_fma_f32 v[168:169], v[22:23], s[2:3], v[168:169] op_sel_hi:[1,0,1]
	s_and_b32 s40, s67, 0xffff0000
	v_pk_fma_f32 v[166:167], v[24:25], s[2:3], v[166:167] op_sel_hi:[1,0,1]
	v_pk_add_f32 v[164:165], v[164:165], v[168:169]
	s_lshl_b32 s2, s67, 16
	v_pk_mul_f32 v[168:169], v[38:39], s[40:41] op_sel_hi:[1,0]
	v_pk_add_f32 v[162:163], v[162:163], v[166:167]
	v_pk_mul_f32 v[166:167], v[40:41], s[40:41] op_sel_hi:[1,0]
	v_pk_fma_f32 v[168:169], v[34:35], s[2:3], v[168:169] op_sel_hi:[1,0,1]
	s_and_b32 s40, s73, 0xffff0000
	v_pk_fma_f32 v[166:167], v[36:37], s[2:3], v[166:167] op_sel_hi:[1,0,1]
	v_pk_add_f32 v[164:165], v[164:165], v[168:169]
	s_lshl_b32 s2, s73, 16
	v_pk_mul_f32 v[168:169], v[46:47], s[40:41] op_sel_hi:[1,0]
	v_pk_add_f32 v[162:163], v[162:163], v[166:167]
	v_pk_mul_f32 v[166:167], v[48:49], s[40:41] op_sel_hi:[1,0]
	v_pk_fma_f32 v[168:169], v[42:43], s[2:3], v[168:169] op_sel_hi:[1,0,1]
	s_and_b32 s40, s74, 0xffff0000
	v_pk_fma_f32 v[166:167], v[44:45], s[2:3], v[166:167] op_sel_hi:[1,0,1]
	v_pk_add_f32 v[164:165], v[164:165], v[168:169]
	s_lshl_b32 s2, s74, 16
	v_pk_mul_f32 v[168:169], v[54:55], s[40:41] op_sel_hi:[1,0]
	s_and_b32 s58, s75, 0xffff0000
	v_pk_fma_f32 v[168:169], v[50:51], s[2:3], v[168:169] op_sel_hi:[1,0,1]
	v_pk_add_f32 v[162:163], v[162:163], v[166:167]
	v_pk_mul_f32 v[166:167], v[56:57], s[40:41] op_sel_hi:[1,0]
	v_pk_add_f32 v[164:165], v[164:165], v[168:169]
	s_lshl_b32 s40, s75, 16
	v_pk_mul_f32 v[168:169], v[62:63], s[58:59] op_sel_hi:[1,0]
	v_pk_fma_f32 v[166:167], v[52:53], s[2:3], v[166:167] op_sel_hi:[1,0,1]
	v_pk_fma_f32 v[168:169], v[58:59], s[40:41], v[168:169] op_sel_hi:[1,0,1]
	v_pk_add_f32 v[162:163], v[162:163], v[166:167]
	v_pk_add_f32 v[164:165], v[164:165], v[168:169]
	v_pk_mul_f32 v[166:167], v[64:65], s[58:59] op_sel_hi:[1,0]
	v_mul_f32_e64 v168, |v164|, s53
	v_exp_f32_e32 v168, v168
	v_pk_fma_f32 v[166:167], v[60:61], s[40:41], v[166:167] op_sel_hi:[1,0,1]
	v_min_f32_e32 v164, 0, v164
	v_pk_add_f32 v[162:163], v[162:163], v[166:167]
	v_add_f32_e32 v168, 1.0, v168
	v_mul_f32_e64 v167, |v165|, s53
	v_exp_f32_e32 v167, v167
	v_log_f32_e32 v168, v168
	v_readlane_b32 s58, v72, 12
	v_readlane_b32 s66, v73, 12
	v_readlane_b32 s67, v70, 13
	v_mul_f32_e32 v166, 0x3f317217, v168
	v_readlane_b32 s73, v71, 13
	v_readlane_b32 s74, v72, 13
	v_mov_b32_e32 v168, 0
	v_sub_f32_e32 v166, v166, v168
	v_sub_f32_e32 v164, v164, v166
	v_add_f32_e32 v166, 1.0, v167
	v_mul_f32_e32 v164, 0x3d800000, v164
	v_readlane_b32 s75, v73, 13
	v_log_f32_e32 v167, v166
	v_max_f32_e32 v166, -1.0, v164
	v_min_f32_e32 v164, 0, v165
	v_mov_b32_e32 v168, 0
	v_mul_f32_e32 v165, 0x3f317217, v167
	v_mul_f32_e32 v159, 0x3d800000, v159
	v_max_f32_e32 v159, -1.0, v159
	v_mul_f32_e64 v167, |v162|, s53
	v_exp_f32_e32 v167, v167
	v_sub_f32_e32 v165, v165, v168
	v_sub_f32_e32 v164, v164, v165
	v_mul_f32_e32 v164, 0x3d800000, v164
	v_add_f32_e32 v165, 1.0, v167
	v_min_f32_e32 v162, 0, v162
	s_nop 0
	v_log_f32_e32 v165, v165
	v_max_f32_e32 v167, -1.0, v164
	v_mov_b32_e32 v168, 0
	v_mul_f32_e32 v164, 0x3f317217, v165
	s_nop 1
	v_mul_f32_e64 v165, |v163|, s53
	v_exp_f32_e32 v165, v165
	v_sub_f32_e32 v164, v164, v168
	v_sub_f32_e32 v162, v162, v164
	v_mul_f32_e32 v162, 0x3d800000, v162
	v_add_f32_e32 v164, 1.0, v165
	s_nop 1
	v_log_f32_e32 v165, v164
	v_max_f32_e32 v164, -1.0, v162
	v_min_f32_e32 v162, 0, v163
	v_mul_f32_e32 v163, 0x3f317217, v165
	s_nop 1
	v_mov_b32_e32 v165, 0
	v_sub_f32_e32 v163, v163, v165
	v_sub_f32_e32 v162, v162, v163
	v_readlane_b32 s40, v70, 12
	v_mul_f32_e32 v162, 0x3d800000, v162
	v_readlane_b32 s41, v71, 12
	s_lshl_b32 s2, s40, 16
	s_and_b32 s40, s40, 0xffff0000
	v_max_f32_e32 v165, -1.0, v162
	v_pk_mul_f32 v[162:163], v[4:5], s[40:41] op_sel_hi:[1,0]
	v_pk_mul_f32 v[168:169], v[2:3], s[40:41] op_sel_hi:[1,0]
	s_and_b32 s40, s41, 0xffff0000
	v_pk_fma_f32 v[162:163], v[28:29], s[2:3], v[162:163] op_sel_hi:[1,0,1]
	v_pk_fma_f32 v[168:169], v[26:27], s[2:3], v[168:169] op_sel_hi:[1,0,1]
	s_lshl_b32 s2, s41, 16
	v_pk_mul_f32 v[172:173], v[10:11], s[40:41] op_sel_hi:[1,0]
	v_pk_add_f32 v[168:169], v[66:67], v[168:169]
	v_pk_mul_f32 v[170:171], v[12:13], s[40:41] op_sel_hi:[1,0]
	v_pk_fma_f32 v[172:173], v[6:7], s[2:3], v[172:173] op_sel_hi:[1,0,1]
	s_and_b32 s40, s58, 0xffff0000
	v_pk_add_f32 v[162:163], v[68:69], v[162:163]
	v_pk_fma_f32 v[170:171], v[8:9], s[2:3], v[170:171] op_sel_hi:[1,0,1]
	v_pk_add_f32 v[168:169], v[168:169], v[172:173]
	s_lshl_b32 s2, s58, 16
	v_pk_mul_f32 v[172:173], v[18:19], s[40:41] op_sel_hi:[1,0]
	v_pk_add_f32 v[162:163], v[162:163], v[170:171]
	v_pk_mul_f32 v[170:171], v[20:21], s[40:41] op_sel_hi:[1,0]
	v_pk_fma_f32 v[172:173], v[14:15], s[2:3], v[172:173] op_sel_hi:[1,0,1]
	s_and_b32 s40, s66, 0xffff0000
	v_pk_fma_f32 v[170:171], v[16:17], s[2:3], v[170:171] op_sel_hi:[1,0,1]
	v_pk_add_f32 v[168:169], v[168:169], v[172:173]
	s_lshl_b32 s2, s66, 16
	v_pk_mul_f32 v[172:173], v[30:31], s[40:41] op_sel_hi:[1,0]
	v_pk_add_f32 v[162:163], v[162:163], v[170:171]
	v_pk_mul_f32 v[170:171], v[32:33], s[40:41] op_sel_hi:[1,0]
	v_pk_fma_f32 v[172:173], v[22:23], s[2:3], v[172:173] op_sel_hi:[1,0,1]
	s_and_b32 s40, s67, 0xffff0000
	v_pk_fma_f32 v[170:171], v[24:25], s[2:3], v[170:171] op_sel_hi:[1,0,1]
	v_pk_add_f32 v[168:169], v[168:169], v[172:173]
	s_lshl_b32 s2, s67, 16
	v_pk_mul_f32 v[172:173], v[38:39], s[40:41] op_sel_hi:[1,0]
	v_pk_add_f32 v[162:163], v[162:163], v[170:171]
	v_pk_mul_f32 v[170:171], v[40:41], s[40:41] op_sel_hi:[1,0]
	v_pk_fma_f32 v[172:173], v[34:35], s[2:3], v[172:173] op_sel_hi:[1,0,1]
	s_and_b32 s40, s73, 0xffff0000
	v_pk_fma_f32 v[170:171], v[36:37], s[2:3], v[170:171] op_sel_hi:[1,0,1]
	v_pk_add_f32 v[168:169], v[168:169], v[172:173]
	s_lshl_b32 s2, s73, 16
	v_pk_mul_f32 v[172:173], v[46:47], s[40:41] op_sel_hi:[1,0]
	v_pk_add_f32 v[162:163], v[162:163], v[170:171]
	v_pk_mul_f32 v[170:171], v[48:49], s[40:41] op_sel_hi:[1,0]
	v_pk_fma_f32 v[172:173], v[42:43], s[2:3], v[172:173] op_sel_hi:[1,0,1]
	s_and_b32 s40, s74, 0xffff0000
	v_pk_fma_f32 v[170:171], v[44:45], s[2:3], v[170:171] op_sel_hi:[1,0,1]
	v_pk_add_f32 v[168:169], v[168:169], v[172:173]
	s_lshl_b32 s2, s74, 16
	v_pk_mul_f32 v[172:173], v[54:55], s[40:41] op_sel_hi:[1,0]
	s_and_b32 s58, s75, 0xffff0000
	v_pk_fma_f32 v[172:173], v[50:51], s[2:3], v[172:173] op_sel_hi:[1,0,1]
	v_pk_add_f32 v[162:163], v[162:163], v[170:171]
	v_pk_mul_f32 v[170:171], v[56:57], s[40:41] op_sel_hi:[1,0]
	v_pk_add_f32 v[168:169], v[168:169], v[172:173]
	s_lshl_b32 s40, s75, 16
	v_pk_mul_f32 v[172:173], v[62:63], s[58:59] op_sel_hi:[1,0]
	v_pk_fma_f32 v[170:171], v[52:53], s[2:3], v[170:171] op_sel_hi:[1,0,1]
	v_pk_fma_f32 v[172:173], v[58:59], s[40:41], v[172:173] op_sel_hi:[1,0,1]
	v_pk_add_f32 v[162:163], v[162:163], v[170:171]
	v_pk_add_f32 v[168:169], v[168:169], v[172:173]
	v_pk_mul_f32 v[170:171], v[64:65], s[58:59] op_sel_hi:[1,0]
	v_mul_f32_e64 v172, |v168|, s53
	v_exp_f32_e32 v172, v172
	v_pk_fma_f32 v[170:171], v[60:61], s[40:41], v[170:171] op_sel_hi:[1,0,1]
	v_min_f32_e32 v168, 0, v168
	v_pk_add_f32 v[162:163], v[162:163], v[170:171]
	v_add_f32_e32 v172, 1.0, v172
	v_mul_f32_e64 v171, |v169|, s53
	v_exp_f32_e32 v171, v171
	v_log_f32_e32 v172, v172
	v_readlane_b32 s58, v72, 14
	v_readlane_b32 s66, v73, 14
	v_readlane_b32 s67, v70, 15
	v_mul_f32_e32 v170, 0x3f317217, v172
	v_readlane_b32 s73, v71, 15
	v_readlane_b32 s74, v72, 15
	v_mov_b32_e32 v172, 0
	v_sub_f32_e32 v170, v170, v172
	v_sub_f32_e32 v168, v168, v170
	v_add_f32_e32 v170, 1.0, v171
	v_mul_f32_e32 v168, 0x3d800000, v168
	v_readlane_b32 s75, v73, 15
	v_log_f32_e32 v171, v170
	v_max_f32_e32 v170, -1.0, v168
	v_min_f32_e32 v168, 0, v169
	v_mov_b32_e32 v172, 0
	v_mul_f32_e32 v169, 0x3f317217, v171
	s_nop 1
	v_mul_f32_e64 v171, |v162|, s53
	v_exp_f32_e32 v171, v171
	v_sub_f32_e32 v169, v169, v172
	v_sub_f32_e32 v168, v168, v169
	v_mul_f32_e32 v168, 0x3d800000, v168
	v_add_f32_e32 v169, 1.0, v171
	v_min_f32_e32 v162, 0, v162
	s_nop 0
	v_log_f32_e32 v169, v169
	v_max_f32_e32 v171, -1.0, v168
	v_mov_b32_e32 v172, 0
	v_mul_f32_e32 v168, 0x3f317217, v169
	s_nop 1
	v_mul_f32_e64 v169, |v163|, s53
	v_exp_f32_e32 v169, v169
	v_sub_f32_e32 v168, v168, v172
	v_sub_f32_e32 v162, v162, v168
	v_mul_f32_e32 v162, 0x3d800000, v162
	v_add_f32_e32 v168, 1.0, v169
	v_max_f32_e32 v178, -1.0, v162
	v_min_f32_e32 v162, 0, v163
	v_log_f32_e32 v168, v168
	s_nop 0
	v_mul_f32_e32 v163, 0x3f317217, v168
	s_nop 1
	v_mov_b32_e32 v168, 0
	v_sub_f32_e32 v163, v163, v168
	v_sub_f32_e32 v162, v162, v163
	v_readlane_b32 s40, v70, 14
	v_mul_f32_e32 v162, 0x3d800000, v162
	v_readlane_b32 s41, v71, 14
	s_lshl_b32 s2, s40, 16
	s_and_b32 s40, s40, 0xffff0000
	v_max_f32_e32 v179, -1.0, v162
	v_pk_mul_f32 v[162:163], v[4:5], s[40:41] op_sel_hi:[1,0]
	v_pk_mul_f32 v[168:169], v[2:3], s[40:41] op_sel_hi:[1,0]
	s_and_b32 s40, s41, 0xffff0000
	v_pk_fma_f32 v[162:163], v[28:29], s[2:3], v[162:163] op_sel_hi:[1,0,1]
	v_pk_fma_f32 v[168:169], v[26:27], s[2:3], v[168:169] op_sel_hi:[1,0,1]
	s_lshl_b32 s2, s41, 16
	v_pk_mul_f32 v[174:175], v[10:11], s[40:41] op_sel_hi:[1,0]
	v_pk_add_f32 v[168:169], v[66:67], v[168:169]
	v_pk_mul_f32 v[172:173], v[12:13], s[40:41] op_sel_hi:[1,0]
	v_pk_fma_f32 v[174:175], v[6:7], s[2:3], v[174:175] op_sel_hi:[1,0,1]
	s_and_b32 s40, s58, 0xffff0000
	v_pk_add_f32 v[162:163], v[68:69], v[162:163]
	v_pk_fma_f32 v[172:173], v[8:9], s[2:3], v[172:173] op_sel_hi:[1,0,1]
	v_pk_add_f32 v[168:169], v[168:169], v[174:175]
	s_lshl_b32 s2, s58, 16
	v_pk_mul_f32 v[174:175], v[18:19], s[40:41] op_sel_hi:[1,0]
	v_pk_add_f32 v[162:163], v[162:163], v[172:173]
	v_pk_mul_f32 v[172:173], v[20:21], s[40:41] op_sel_hi:[1,0]
	v_pk_fma_f32 v[174:175], v[14:15], s[2:3], v[174:175] op_sel_hi:[1,0,1]
	s_and_b32 s40, s66, 0xffff0000
	v_pk_fma_f32 v[172:173], v[16:17], s[2:3], v[172:173] op_sel_hi:[1,0,1]
	v_pk_add_f32 v[168:169], v[168:169], v[174:175]
	s_lshl_b32 s2, s66, 16
	v_pk_mul_f32 v[174:175], v[30:31], s[40:41] op_sel_hi:[1,0]
	v_pk_add_f32 v[162:163], v[162:163], v[172:173]
	v_pk_mul_f32 v[172:173], v[32:33], s[40:41] op_sel_hi:[1,0]
	v_pk_fma_f32 v[174:175], v[22:23], s[2:3], v[174:175] op_sel_hi:[1,0,1]
	s_and_b32 s40, s67, 0xffff0000
	v_pk_fma_f32 v[172:173], v[24:25], s[2:3], v[172:173] op_sel_hi:[1,0,1]
	v_pk_add_f32 v[168:169], v[168:169], v[174:175]
	s_lshl_b32 s2, s67, 16
	v_pk_mul_f32 v[174:175], v[38:39], s[40:41] op_sel_hi:[1,0]
	v_pk_add_f32 v[162:163], v[162:163], v[172:173]
	v_pk_mul_f32 v[172:173], v[40:41], s[40:41] op_sel_hi:[1,0]
	v_pk_fma_f32 v[174:175], v[34:35], s[2:3], v[174:175] op_sel_hi:[1,0,1]
	s_and_b32 s40, s73, 0xffff0000
	v_pk_fma_f32 v[172:173], v[36:37], s[2:3], v[172:173] op_sel_hi:[1,0,1]
	v_pk_add_f32 v[168:169], v[168:169], v[174:175]
	s_lshl_b32 s2, s73, 16
	v_pk_mul_f32 v[174:175], v[46:47], s[40:41] op_sel_hi:[1,0]
	v_pk_add_f32 v[162:163], v[162:163], v[172:173]
	v_pk_mul_f32 v[172:173], v[48:49], s[40:41] op_sel_hi:[1,0]
	v_pk_fma_f32 v[174:175], v[42:43], s[2:3], v[174:175] op_sel_hi:[1,0,1]
	s_and_b32 s40, s74, 0xffff0000
	v_pk_fma_f32 v[172:173], v[44:45], s[2:3], v[172:173] op_sel_hi:[1,0,1]
	v_pk_add_f32 v[168:169], v[168:169], v[174:175]
	s_lshl_b32 s2, s74, 16
	v_pk_mul_f32 v[174:175], v[54:55], s[40:41] op_sel_hi:[1,0]
	s_and_b32 s58, s75, 0xffff0000
	v_pk_fma_f32 v[174:175], v[50:51], s[2:3], v[174:175] op_sel_hi:[1,0,1]
	v_pk_add_f32 v[162:163], v[162:163], v[172:173]
	v_pk_mul_f32 v[172:173], v[56:57], s[40:41] op_sel_hi:[1,0]
	v_pk_add_f32 v[168:169], v[168:169], v[174:175]
	s_lshl_b32 s40, s75, 16
	v_pk_mul_f32 v[174:175], v[62:63], s[58:59] op_sel_hi:[1,0]
	v_pk_fma_f32 v[172:173], v[52:53], s[2:3], v[172:173] op_sel_hi:[1,0,1]
	v_pk_fma_f32 v[174:175], v[58:59], s[40:41], v[174:175] op_sel_hi:[1,0,1]
	v_pk_add_f32 v[162:163], v[162:163], v[172:173]
	v_pk_add_f32 v[168:169], v[168:169], v[174:175]
	v_pk_mul_f32 v[172:173], v[64:65], s[58:59] op_sel_hi:[1,0]
	v_mul_f32_e64 v174, |v168|, s53
	v_exp_f32_e32 v174, v174
	v_pk_fma_f32 v[172:173], v[60:61], s[40:41], v[172:173] op_sel_hi:[1,0,1]
	v_add_f32_e32 v174, 1.0, v174
	s_nop 1
	v_log_f32_e32 v176, v174
	v_pk_add_f32 v[174:175], v[162:163], v[172:173]
	v_min_f32_e32 v162, 0, v168
	v_mul_f32_e64 v168, |v169|, s53
	v_mul_f32_e32 v163, 0x3f317217, v176
	v_exp_f32_e32 v168, v168
	v_mov_b32_e32 v172, 0
	s_nop 0
	v_sub_f32_e32 v163, v163, v172
	v_sub_f32_e32 v162, v162, v163
	v_add_f32_e32 v163, 1.0, v168
	v_pk_add_f32 v[176:177], v[74:75], 0 op_sel_hi:[1,0]
	v_mul_f32_e64 v74, |v174|, s53
	v_log_f32_e32 v163, v163
	v_exp_f32_e32 v74, v74
	v_mul_f32_e32 v162, 0x3d800000, v162
	v_max_f32_e32 v186, -1.0, v162
	v_mul_f32_e32 v168, 0x3f317217, v163
	v_add_f32_e32 v74, 1.0, v74
	v_min_f32_e32 v162, 0, v169
	v_mov_b32_e32 v163, v168
	v_mov_b32_e32 v168, 0
	v_sub_f32_e32 v163, v163, v168
	v_sub_f32_e32 v162, v162, v163
	v_pk_add_f32 v[172:173], v[176:177], v[80:81]
	v_log_f32_e32 v80, v74
	v_mul_f32_e32 v162, 0x3d800000, v162
	v_pk_add_f32 v[168:169], v[172:173], v[152:153]
	v_max_f32_e32 v187, -1.0, v162
	v_pk_add_f32 v[162:163], v[168:169], v[156:157]
	v_pk_add_f32 v[160:161], v[162:163], v[160:161]
	v_min_f32_e32 v81, 0, v174
	v_pk_add_f32 v[156:157], v[160:161], v[166:167]
	v_mul_f32_e32 v166, 0x3f317217, v80
	v_mov_b32_e32 v80, v166
	v_mul_f32_e64 v166, |v175|, s53
	v_exp_f32_e32 v166, v166
	v_mov_b32_e32 v167, 0
	v_sub_f32_e32 v80, v80, v167
	v_sub_f32_e32 v80, v81, v80
	v_add_f32_e32 v81, 1.0, v166
	v_pk_add_f32 v[152:153], v[156:157], v[170:171]
	v_mul_f32_e32 v80, 0x3d800000, v80
	v_log_f32_e32 v81, v81
	v_min_f32_e32 v166, 0, v175
	v_pk_add_f32 v[174:175], v[190:191], v[78:79]
	v_max_f32_e32 v80, -1.0, v80
	v_mul_f32_e32 v167, 0x3f317217, v81
	v_pk_add_f32 v[170:171], v[174:175], v[150:151]
	v_pk_add_f32 v[74:75], v[152:153], v[186:187]
	v_mov_b32_e32 v81, v167
	v_mov_b32_e32 v167, 0
	v_sub_f32_e32 v81, v81, v167
	v_sub_f32_e32 v81, v166, v81
	v_pk_add_f32 v[166:167], v[170:171], v[154:155]
	v_mul_f32_e32 v81, 0x3d800000, v81
	v_pk_add_f32 v[158:159], v[166:167], v[158:159]
	v_max_f32_e32 v81, -1.0, v81
	v_pk_add_f32 v[154:155], v[158:159], v[164:165]
	s_ashr_i32 s41, s72, 31
	v_pk_add_f32 v[150:151], v[154:155], v[178:179]
	s_mov_b32 s40, s72
	v_pk_add_f32 v[76:77], v[150:151], v[80:81]
	ds_write_b128 v85, v[74:77]
	s_waitcnt lgkmcnt(0)
	s_barrier
	ds_read_b128 v[78:81], v97
	ds_read_b128 v[186:189], v97 offset:1024
	s_lshl_b64 s[66:67], s[40:41], 11
	s_andn2_b64 vcc, exec, s[60:61]
	s_waitcnt lgkmcnt(1)
	v_pk_add_f32 v[80:81], v[80:81], 0 op_sel_hi:[1,0]
	v_pk_add_f32 v[78:79], v[78:79], 0 op_sel_hi:[1,0]
	v_cndmask_b32_e64 v179, 0, v81, s[6:7]
	v_cndmask_b32_e64 v165, 0, v79, s[6:7]
	v_cndmask_b32_e64 v164, 0, v78, s[6:7]
	v_cndmask_b32_e64 v178, 0, v80, s[6:7]
	s_waitcnt lgkmcnt(0)
	v_pk_add_f32 v[192:193], v[80:81], v[188:189]
	v_pk_add_f32 v[194:195], v[78:79], v[186:187]
	ds_read_b128 v[78:81], v97 offset:2048
	v_pk_add_f32 v[186:187], v[186:187], v[164:165]
	v_pk_add_f32 v[188:189], v[188:189], v[178:179]
	v_cndmask_b32_e64 v165, v165, v187, s[8:9]
	v_cndmask_b32_e64 v164, v164, v186, s[8:9]
	v_cndmask_b32_e64 v179, v179, v189, s[8:9]
	v_cndmask_b32_e64 v178, v178, v188, s[8:9]
	ds_read_b128 v[186:189], v97 offset:3072
	s_waitcnt lgkmcnt(1)
	v_pk_add_f32 v[192:193], v[192:193], v[80:81]
	v_pk_add_f32 v[194:195], v[194:195], v[78:79]
	v_pk_add_f32 v[78:79], v[78:79], v[164:165]
	v_pk_add_f32 v[80:81], v[80:81], v[178:179]
	v_cndmask_b32_e64 v165, v165, v79, s[10:11]
	v_cndmask_b32_e64 v164, v164, v78, s[10:11]
	v_cndmask_b32_e64 v179, v179, v81, s[10:11]
	v_cndmask_b32_e64 v178, v178, v80, s[10:11]
	ds_read_b128 v[78:81], v97 offset:4096
	s_waitcnt lgkmcnt(1)
	v_pk_add_f32 v[192:193], v[192:193], v[188:189]
	v_pk_add_f32 v[194:195], v[194:195], v[186:187]
	v_pk_add_f32 v[186:187], v[186:187], v[164:165]
	v_pk_add_f32 v[188:189], v[188:189], v[178:179]
	v_cndmask_b32_e64 v165, v165, v187, s[12:13]
	v_cndmask_b32_e64 v164, v164, v186, s[12:13]
	v_cndmask_b32_e64 v179, v179, v189, s[12:13]
	v_cndmask_b32_e64 v178, v178, v188, s[12:13]
	ds_read_b128 v[186:189], v97 offset:5120
	s_waitcnt lgkmcnt(1)
	v_pk_add_f32 v[192:193], v[192:193], v[80:81]
	v_pk_add_f32 v[194:195], v[194:195], v[78:79]
	v_pk_add_f32 v[78:79], v[78:79], v[164:165]
	v_pk_add_f32 v[80:81], v[80:81], v[178:179]
	v_cndmask_b32_e64 v165, v165, v79, s[14:15]
	v_cndmask_b32_e64 v164, v164, v78, s[14:15]
	v_cndmask_b32_e64 v179, v179, v81, s[14:15]
	v_cndmask_b32_e64 v178, v178, v80, s[14:15]
	ds_read_b128 v[78:81], v97 offset:6144
	s_waitcnt lgkmcnt(1)
	v_pk_add_f32 v[192:193], v[192:193], v[188:189]
	v_pk_add_f32 v[194:195], v[194:195], v[186:187]
	v_pk_add_f32 v[186:187], v[186:187], v[164:165]
	v_pk_add_f32 v[188:189], v[188:189], v[178:179]
	v_cndmask_b32_e64 v165, v165, v187, s[16:17]
	v_cndmask_b32_e64 v164, v164, v186, s[16:17]
	v_cndmask_b32_e64 v179, v179, v189, s[16:17]
	v_cndmask_b32_e64 v178, v178, v188, s[16:17]
	ds_read_b128 v[186:189], v97 offset:7168
	s_waitcnt lgkmcnt(1)
	v_pk_add_f32 v[194:195], v[194:195], v[78:79]
	v_pk_add_f32 v[78:79], v[78:79], v[164:165]
	v_pk_add_f32 v[192:193], v[192:193], v[80:81]
	v_cndmask_b32_e64 v165, v165, v79, s[18:19]
	v_cndmask_b32_e64 v164, v164, v78, s[18:19]
	s_waitcnt lgkmcnt(0)
	v_pk_add_f32 v[78:79], v[194:195], v[186:187]
	v_pk_add_f32 v[186:187], v[186:187], v[164:165]
	v_pk_add_f32 v[80:81], v[80:81], v[178:179]
	v_cndmask_b32_e64 v186, v164, v186, s[20:21]
	v_add_f32_e32 v176, v176, v186
	v_mul_f32_e32 v195, 0x3fb8aa3b, v176
	v_exp_f32_e32 v195, v195
	v_mul_f32_e32 v176, 0xbfb8aa3b, v176
	v_exp_f32_e32 v176, v176
	s_waitcnt vmcnt(8)
	v_lshlrev_b32_e32 v164, 16, v126
	v_cndmask_b32_e64 v187, v165, v187, s[20:21]
	v_mul_f32_e32 v164, 0x3d800000, v164
	v_cndmask_b32_e64 v179, v179, v81, s[18:19]
	v_cndmask_b32_e64 v178, v178, v80, s[18:19]
	v_pk_add_f32 v[80:81], v[192:193], v[188:189]
	v_lshlrev_b32_e32 v192, 16, v104
	v_mul_f32_e32 v195, v164, v195
	v_add_f32_e32 v164, v177, v187
	v_mul_f32_e32 v192, v176, v192
	v_mul_f32_e32 v176, 0x3fb8aa3b, v164
	v_mul_f32_e32 v164, 0xbfb8aa3b, v164
	v_exp_f32_e32 v164, v164
	v_exp_f32_e32 v176, v176
	v_pk_add_f32 v[188:189], v[188:189], v[178:179]
	v_and_b32_e32 v165, 0xffff0000, v126
	v_cndmask_b32_e64 v178, v178, v188, s[20:21]
	v_and_b32_e32 v193, 0xffff0000, v104
	v_mul_f32_e32 v165, 0x3d800000, v165
	v_mul_f32_e32 v193, v164, v193
	v_add_f32_e32 v164, v190, v178
	v_mul_f32_e32 v176, v165, v176
	v_mul_f32_e32 v165, 0x3fb8aa3b, v164
	v_mul_f32_e32 v164, 0xbfb8aa3b, v164
	v_exp_f32_e32 v164, v164
	v_exp_f32_e32 v165, v165
	v_cndmask_b32_e64 v179, v179, v189, s[20:21]
	v_lshlrev_b32_e32 v188, 16, v127
	v_lshlrev_b32_e32 v194, 16, v105
	v_mul_f32_e32 v177, 0x3d800000, v188
	v_mul_f32_e32 v188, v164, v194
	v_add_f32_e32 v164, v191, v179
	v_mul_f32_e32 v177, v177, v165
	v_mul_f32_e32 v165, 0x3fb8aa3b, v164
	v_mul_f32_e32 v164, 0xbfb8aa3b, v164
	v_mul_f32_e32 v81, 0x3fb8aa3b, v81
	v_exp_f32_e32 v191, v165
	v_exp_f32_e32 v164, v164
	v_add_f32_e32 v172, v172, v186
	v_exp_f32_e32 v81, v81
	v_mul_f32_e32 v194, 0x3fb8aa3b, v172
	v_mul_f32_e32 v172, 0xbfb8aa3b, v172
	v_and_b32_e32 v189, 0xffff0000, v127
	v_exp_f32_e32 v172, v172
	v_mul_f32_e32 v189, 0x3d800000, v189
	v_mul_f32_e32 v189, v189, v191
	v_mul_f32_e32 v191, v164, v196
	v_cvt_pk_bf16_f32 v176, v195, v176
	v_cvt_pk_bf16_f32 v177, v177, v189
	v_mul_f32_e32 v164, v81, v191
	ds_write_b64 v101, v[176:177]
	v_cvt_pk_bf16_f32 v176, v192, v193
	v_cvt_pk_bf16_f32 v177, v188, v191
	s_waitcnt vmcnt(13)
	v_lshlrev_b32_e32 v191, 16, v108
	v_mul_f32_e32 v78, 0x3fb8aa3b, v78
	v_mul_f32_e32 v191, v172, v191
	v_add_f32_e32 v172, v173, v187
	v_exp_f32_e32 v78, v78
	v_mul_f32_e32 v173, 0x3fb8aa3b, v172
	v_mul_f32_e32 v172, 0xbfb8aa3b, v172
	v_exp_f32_e32 v173, v173
	v_exp_f32_e32 v172, v172
	ds_write_b64 v101, v[176:177] offset:33792
	s_waitcnt vmcnt(12)
	v_and_b32_e32 v177, 0xffff0000, v114
	v_mul_f32_e32 v80, 0x3fb8aa3b, v80
	v_mul_f32_e32 v197, v78, v192
	v_and_b32_e32 v192, 0xffff0000, v108
	v_mul_f32_e32 v177, 0x3d800000, v177
	v_mul_f32_e32 v79, 0x3fb8aa3b, v79
	v_exp_f32_e32 v80, v80
	v_mul_f32_e32 v173, v177, v173
	v_mul_f32_e32 v177, v172, v192
	v_add_f32_e32 v172, v174, v178
	v_exp_f32_e32 v79, v79
	v_mul_f32_e32 v174, 0x3fb8aa3b, v172
	v_mul_f32_e32 v172, 0xbfb8aa3b, v172
	v_exp_f32_e32 v174, v174
	v_exp_f32_e32 v172, v172
	v_mul_f32_e32 v165, v80, v188
	v_lshlrev_b32_e32 v188, 16, v115
	v_mul_f32_e32 v190, v79, v193
	v_lshlrev_b32_e32 v193, 16, v109
	v_mul_f32_e32 v188, 0x3d800000, v188
	v_mul_f32_e32 v174, v188, v174
	v_mul_f32_e32 v188, v172, v193
	v_add_f32_e32 v172, v175, v179
	v_mul_f32_e32 v175, 0x3fb8aa3b, v172
	v_mul_f32_e32 v172, 0xbfb8aa3b, v172
	v_exp_f32_e32 v194, v194
	v_exp_f32_e32 v175, v175
	v_exp_f32_e32 v172, v172
	v_lshlrev_b32_e32 v176, 16, v114
	v_and_b32_e32 v189, 0xffff0000, v115
	v_and_b32_e32 v195, 0xffff0000, v109
	v_mul_f32_e32 v176, 0x3d800000, v176
	v_mul_f32_e32 v189, 0x3d800000, v189
	v_mul_f32_e32 v176, v176, v194
	v_mul_f32_e32 v175, v189, v175
	v_mul_f32_e32 v189, v172, v195
	v_cvt_pk_bf16_f32 v172, v176, v173
	v_cvt_pk_bf16_f32 v173, v174, v175
	v_add_f32_e32 v168, v168, v186
	v_mul_f32_e32 v195, v81, v189
	ds_write_b64 v101, v[172:173] offset:528
	v_cvt_pk_bf16_f32 v172, v191, v177
	v_cvt_pk_bf16_f32 v173, v188, v189
	v_mul_f32_e32 v189, 0x3fb8aa3b, v168
	v_mul_f32_e32 v168, 0xbfb8aa3b, v168
	v_exp_f32_e32 v168, v168
	s_waitcnt vmcnt(10)
	v_lshlrev_b32_e32 v176, 16, v120
	ds_write_b64 v101, v[172:173] offset:34320
	v_and_b32_e32 v173, 0xffff0000, v118
	v_mul_f32_e32 v176, v168, v176
	v_add_f32_e32 v168, v169, v187
	v_mul_f32_e32 v169, 0x3fb8aa3b, v168
	v_mul_f32_e32 v168, 0xbfb8aa3b, v168
	v_exp_f32_e32 v169, v169
	v_exp_f32_e32 v168, v168
	v_mul_f32_e32 v192, v79, v177
	v_and_b32_e32 v177, 0xffff0000, v120
	v_mul_f32_e32 v173, 0x3d800000, v173
	v_mul_f32_e32 v169, v173, v169
	v_mul_f32_e32 v173, v168, v177
	v_add_f32_e32 v168, v170, v178
	v_mul_f32_e32 v170, 0x3fb8aa3b, v168
	v_mul_f32_e32 v168, 0xbfb8aa3b, v168
	v_exp_f32_e32 v170, v170
	v_exp_f32_e32 v168, v168
	v_lshlrev_b32_e32 v174, 16, v119
	v_mul_f32_e32 v193, v80, v188
	v_lshlrev_b32_e32 v188, 16, v121
	v_mul_f32_e32 v174, 0x3d800000, v174
	v_mul_f32_e32 v170, v174, v170
	v_mul_f32_e32 v174, v168, v188
	v_add_f32_e32 v168, v171, v179
	v_mul_f32_e32 v171, 0x3fb8aa3b, v168
	v_mul_f32_e32 v168, 0xbfb8aa3b, v168
	v_exp_f32_e32 v189, v189
	v_exp_f32_e32 v171, v171
	v_exp_f32_e32 v168, v168
	v_lshlrev_b32_e32 v172, 16, v118
	v_and_b32_e32 v175, 0xffff0000, v119
	v_mul_f32_e32 v194, v78, v191
	v_and_b32_e32 v191, 0xffff0000, v121
	v_mul_f32_e32 v172, 0x3d800000, v172
	v_mul_f32_e32 v175, 0x3d800000, v175
	v_mul_f32_e32 v172, v172, v189
	v_mul_f32_e32 v171, v175, v171
	v_mul_f32_e32 v175, v168, v191
	v_cvt_pk_bf16_f32 v168, v172, v169
	v_cvt_pk_bf16_f32 v169, v170, v171
	v_add_f32_e32 v162, v162, v186
	v_mul_f32_e32 v191, v81, v175
	ds_write_b64 v101, v[168:169] offset:1056
	v_cvt_pk_bf16_f32 v168, v176, v173
	v_cvt_pk_bf16_f32 v169, v174, v175
	v_mul_f32_e32 v175, 0x3fb8aa3b, v162
	v_mul_f32_e32 v162, 0xbfb8aa3b, v162
	v_exp_f32_e32 v162, v162
	s_waitcnt vmcnt(3)
	v_lshlrev_b32_e32 v172, 16, v140
	ds_write_b64 v101, v[168:169] offset:34848
	v_and_b32_e32 v169, 0xffff0000, v130
	v_mul_f32_e32 v172, v162, v172
	v_add_f32_e32 v162, v163, v187
	v_mul_f32_e32 v163, 0x3fb8aa3b, v162
	v_mul_f32_e32 v162, 0xbfb8aa3b, v162
	v_exp_f32_e32 v163, v163
	v_exp_f32_e32 v162, v162
	v_mul_f32_e32 v177, v79, v173
	v_and_b32_e32 v173, 0xffff0000, v140
	v_mul_f32_e32 v169, 0x3d800000, v169
	v_mul_f32_e32 v163, v169, v163
	v_mul_f32_e32 v169, v162, v173
	v_add_f32_e32 v162, v166, v178
	v_mul_f32_e32 v166, 0x3fb8aa3b, v162
	v_mul_f32_e32 v162, 0xbfb8aa3b, v162
	v_exp_f32_e32 v166, v166
	v_exp_f32_e32 v162, v162
	v_lshlrev_b32_e32 v170, 16, v131
	v_mul_f32_e32 v188, v80, v174
	v_lshlrev_b32_e32 v174, 16, v141
	v_mul_f32_e32 v170, 0x3d800000, v170
	v_mul_f32_e32 v166, v170, v166
	v_mul_f32_e32 v170, v162, v174
	v_add_f32_e32 v162, v167, v179
	v_mul_f32_e32 v167, 0x3fb8aa3b, v162
	v_mul_f32_e32 v162, 0xbfb8aa3b, v162
	v_exp_f32_e32 v175, v175
	v_exp_f32_e32 v167, v167
	v_exp_f32_e32 v162, v162
	v_lshlrev_b32_e32 v168, 16, v130
	v_and_b32_e32 v171, 0xffff0000, v131
	v_mul_f32_e32 v189, v78, v176
	v_and_b32_e32 v176, 0xffff0000, v141
	v_mul_f32_e32 v168, 0x3d800000, v168
	v_mul_f32_e32 v171, 0x3d800000, v171
	v_mul_f32_e32 v168, v168, v175
	v_mul_f32_e32 v167, v171, v167
	v_mul_f32_e32 v171, v162, v176
	v_cvt_pk_bf16_f32 v162, v168, v163
	v_cvt_pk_bf16_f32 v163, v166, v167
	v_add_f32_e32 v160, v160, v186
	v_mul_f32_e32 v176, v81, v171
	ds_write_b64 v101, v[162:163] offset:1584
	v_cvt_pk_bf16_f32 v162, v172, v169
	v_cvt_pk_bf16_f32 v163, v170, v171
	v_mul_f32_e32 v171, 0x3fb8aa3b, v160
	v_mul_f32_e32 v160, 0xbfb8aa3b, v160
	v_exp_f32_e32 v160, v160
	v_lshlrev_b32_e32 v168, 16, v134
	v_add_f32_e32 v161, v161, v187
	ds_write_b64 v101, v[162:163] offset:35376
	v_mul_f32_e32 v160, v160, v168
	v_mul_f32_e32 v168, 0x3fb8aa3b, v161
	v_exp_f32_e32 v168, v168
	v_and_b32_e32 v163, 0xffff0000, v132
	v_mul_f32_e32 v163, 0x3d800000, v163
	v_add_f32_e32 v158, v158, v178
	v_mul_f32_e32 v163, v163, v168
	v_mul_f32_e32 v168, 0x3fb8aa3b, v158
	v_mul_f32_e32 v158, 0xbfb8aa3b, v158
	v_exp_f32_e32 v168, v168
	v_exp_f32_e32 v158, v158
	v_lshlrev_b32_e32 v166, 16, v133
	v_mul_f32_e32 v174, v80, v170
	v_lshlrev_b32_e32 v170, 16, v135
	v_mul_f32_e32 v166, 0x3d800000, v166
	v_mul_f32_e32 v166, v166, v168
	v_mul_f32_e32 v168, v158, v170
	v_add_f32_e32 v158, v159, v179
	v_mul_f32_e32 v159, 0x3fb8aa3b, v158
	v_exp_f32_e32 v159, v159
	v_mul_f32_e32 v158, 0xbfb8aa3b, v158
	v_exp_f32_e32 v171, v171
	v_mul_f32_e32 v161, 0xbfb8aa3b, v161
	v_exp_f32_e32 v158, v158
	v_and_b32_e32 v167, 0xffff0000, v133
	v_exp_f32_e32 v161, v161
	v_lshlrev_b32_e32 v162, 16, v132
	v_mul_f32_e32 v167, 0x3d800000, v167
	v_mul_f32_e32 v175, v78, v172
	v_and_b32_e32 v172, 0xffff0000, v135
	v_mul_f32_e32 v162, 0x3d800000, v162
	v_mul_f32_e32 v159, v167, v159
	v_mul_f32_e32 v173, v79, v169
	v_and_b32_e32 v169, 0xffff0000, v134
	v_mul_f32_e32 v162, v162, v171
	v_mul_f32_e32 v167, v158, v172
	v_cvt_pk_bf16_f32 v158, v162, v163
	v_cvt_pk_bf16_f32 v159, v166, v159
	v_add_f32_e32 v156, v156, v186
	v_mul_f32_e32 v161, v161, v169
	v_mul_f32_e32 v172, v81, v167
	ds_write_b64 v101, v[158:159] offset:2112
	v_cvt_pk_bf16_f32 v158, v160, v161
	v_cvt_pk_bf16_f32 v159, v168, v167
	v_mul_f32_e32 v167, 0x3fb8aa3b, v156
	v_mul_f32_e32 v156, 0xbfb8aa3b, v156
	v_exp_f32_e32 v156, v156
	s_waitcnt vmcnt(2)
	v_lshlrev_b32_e32 v162, 16, v142
	v_add_f32_e32 v157, v157, v187
	ds_write_b64 v101, v[158:159] offset:35904
	v_mul_f32_e32 v156, v156, v162
	v_mul_f32_e32 v162, 0x3fb8aa3b, v157
	v_exp_f32_e32 v162, v162
	v_and_b32_e32 v159, 0xffff0000, v136
	v_mul_f32_e32 v159, 0x3d800000, v159
	v_add_f32_e32 v154, v154, v178
	v_mul_f32_e32 v159, v159, v162
	v_mul_f32_e32 v162, 0x3fb8aa3b, v154
	v_mul_f32_e32 v154, 0xbfb8aa3b, v154
	v_exp_f32_e32 v162, v162
	v_exp_f32_e32 v154, v154
	v_mul_f32_e32 v171, v78, v160
	v_lshlrev_b32_e32 v160, 16, v137
	v_lshlrev_b32_e32 v166, 16, v143
	v_mul_f32_e32 v160, 0x3d800000, v160
	v_mul_f32_e32 v160, v160, v162
	v_mul_f32_e32 v162, v154, v166
	v_add_f32_e32 v154, v155, v179
	v_mul_f32_e32 v155, 0x3fb8aa3b, v154
	v_exp_f32_e32 v155, v155
	v_mul_f32_e32 v154, 0xbfb8aa3b, v154
	v_exp_f32_e32 v167, v167
	v_mul_f32_e32 v157, 0xbfb8aa3b, v157
	v_exp_f32_e32 v154, v154
	v_mul_f32_e32 v169, v79, v161
	v_and_b32_e32 v161, 0xffff0000, v137
	v_exp_f32_e32 v157, v157
	v_lshlrev_b32_e32 v158, 16, v136
	v_mul_f32_e32 v161, 0x3d800000, v161
	v_mul_f32_e32 v170, v80, v168
	v_and_b32_e32 v168, 0xffff0000, v143
	v_mul_f32_e32 v158, 0x3d800000, v158
	v_mul_f32_e32 v155, v161, v155
	v_and_b32_e32 v163, 0xffff0000, v142
	v_mul_f32_e32 v158, v158, v167
	v_mul_f32_e32 v161, v154, v168
	v_cvt_pk_bf16_f32 v154, v158, v159
	v_cvt_pk_bf16_f32 v155, v160, v155
	v_add_f32_e32 v152, v152, v186
	v_mul_f32_e32 v157, v157, v163
	v_mul_f32_e32 v168, v81, v161
	ds_write_b64 v101, v[154:155] offset:2640
	v_cvt_pk_bf16_f32 v154, v156, v157
	v_cvt_pk_bf16_f32 v155, v162, v161
	v_mul_f32_e32 v161, 0x3fb8aa3b, v152
	v_mul_f32_e32 v152, 0xbfb8aa3b, v152
	v_exp_f32_e32 v152, v152
	v_lshlrev_b32_e32 v158, 16, v144
	v_add_f32_e32 v153, v153, v187
	ds_write_b64 v101, v[154:155] offset:36432
	v_mul_f32_e32 v152, v152, v158
	v_mul_f32_e32 v158, 0x3fb8aa3b, v153
	v_exp_f32_e32 v158, v158
	v_and_b32_e32 v155, 0xffff0000, v138
	v_mul_f32_e32 v155, 0x3d800000, v155
	v_add_f32_e32 v150, v150, v178
	v_mul_f32_e32 v155, v155, v158
	v_mul_f32_e32 v158, 0x3fb8aa3b, v150
	v_mul_f32_e32 v150, 0xbfb8aa3b, v150
	v_exp_f32_e32 v158, v158
	v_exp_f32_e32 v150, v150
	v_mul_f32_e32 v167, v78, v156
	v_lshlrev_b32_e32 v156, 16, v139
	v_lshlrev_b32_e32 v160, 16, v145
	v_mul_f32_e32 v156, 0x3d800000, v156
	v_mul_f32_e32 v156, v156, v158
	v_mul_f32_e32 v158, v150, v160
	v_add_f32_e32 v150, v151, v179
	v_mul_f32_e32 v151, 0x3fb8aa3b, v150
	v_exp_f32_e32 v151, v151
	v_mul_f32_e32 v150, 0xbfb8aa3b, v150
	v_exp_f32_e32 v161, v161
	v_mul_f32_e32 v153, 0xbfb8aa3b, v153
	v_exp_f32_e32 v150, v150
	v_mul_f32_e32 v163, v79, v157
	v_and_b32_e32 v157, 0xffff0000, v139
	v_exp_f32_e32 v153, v153
	v_lshlrev_b32_e32 v154, 16, v138
	v_mul_f32_e32 v157, 0x3d800000, v157
	v_mul_f32_e32 v166, v80, v162
	v_and_b32_e32 v162, 0xffff0000, v145
	v_mul_f32_e32 v154, 0x3d800000, v154
	v_mul_f32_e32 v151, v157, v151
	v_and_b32_e32 v159, 0xffff0000, v144
	v_mul_f32_e32 v154, v154, v161
	v_mul_f32_e32 v157, v150, v162
	v_cvt_pk_bf16_f32 v150, v154, v155
	v_cvt_pk_bf16_f32 v151, v156, v151
	v_add_f32_e32 v74, v74, v186
	v_mul_f32_e32 v153, v153, v159
	v_mul_f32_e32 v162, v81, v157
	ds_write_b64 v101, v[150:151] offset:3168
	v_cvt_pk_bf16_f32 v150, v152, v153
	v_cvt_pk_bf16_f32 v151, v158, v157
	v_mul_f32_e32 v157, 0x3fb8aa3b, v74
	v_mul_f32_e32 v74, 0xbfb8aa3b, v74
	v_exp_f32_e32 v74, v74
	s_waitcnt vmcnt(0)
	v_lshlrev_b32_e32 v154, 16, v148
	ds_write_b64 v101, v[150:151] offset:36960
	v_and_b32_e32 v151, 0xffff0000, v146
	v_mul_f32_e32 v154, v74, v154
	v_add_f32_e32 v74, v75, v187
	v_mul_f32_e32 v75, 0x3fb8aa3b, v74
	v_mul_f32_e32 v74, 0xbfb8aa3b, v74
	v_exp_f32_e32 v75, v75
	v_exp_f32_e32 v74, v74
	v_and_b32_e32 v155, 0xffff0000, v148
	v_mul_f32_e32 v151, 0x3d800000, v151
	v_mul_f32_e32 v75, v151, v75
	v_mul_f32_e32 v151, v74, v155
	v_add_f32_e32 v74, v76, v178
	v_mul_f32_e32 v76, 0x3fb8aa3b, v74
	v_mul_f32_e32 v74, 0xbfb8aa3b, v74
	v_exp_f32_e32 v76, v76
	v_exp_f32_e32 v74, v74
	v_mul_f32_e32 v161, v78, v152
	v_lshlrev_b32_e32 v152, 16, v147
	v_lshlrev_b32_e32 v156, 16, v149
	v_mul_f32_e32 v152, 0x3d800000, v152
	v_mul_f32_e32 v76, v152, v76
	v_mul_f32_e32 v152, v74, v156
	v_add_f32_e32 v74, v77, v179
	v_mul_f32_e32 v77, 0x3fb8aa3b, v74
	v_mul_f32_e32 v74, 0xbfb8aa3b, v74
	v_exp_f32_e32 v157, v157
	v_exp_f32_e32 v77, v77
	v_exp_f32_e32 v74, v74
	v_mul_f32_e32 v159, v79, v153
	v_lshlrev_b32_e32 v150, 16, v146
	v_and_b32_e32 v153, 0xffff0000, v147
	v_mul_f32_e32 v160, v80, v158
	v_and_b32_e32 v158, 0xffff0000, v149
	v_mul_f32_e32 v150, 0x3d800000, v150
	v_mul_f32_e32 v153, 0x3d800000, v153
	v_mul_f32_e32 v150, v150, v157
	v_mul_f32_e32 v77, v153, v77
	v_mul_f32_e32 v153, v74, v158
	v_cvt_pk_bf16_f32 v74, v150, v75
	v_mul_f32_e32 v155, v79, v151
	v_cvt_pk_bf16_f32 v75, v76, v77
	ds_write_b64 v101, v[74:75] offset:3696
	v_cvt_pk_bf16_f32 v74, v154, v151
	v_lshl_add_u64 v[150:151], v[128:129], 0, s[66:67]
	v_mul_f32_e32 v156, v80, v152
	v_mul_f32_e32 v158, v81, v153
	v_cvt_pk_bf16_f32 v75, v152, v153
	v_or_b32_e32 v152, v150, v84
	v_mov_b32_e32 v153, v151
	v_lshl_add_u64 v[152:153], v[152:153], 4, s[56:57]
	v_mul_f32_e32 v157, v78, v154
	ds_write_b64 v101, v[74:75] offset:37488
	v_cvt_pk_bf16_f32 v74, v197, v194
	v_cvt_pk_bf16_f32 v75, v189, v175
	v_cvt_pk_bf16_f32 v76, v171, v167
	v_cvt_pk_bf16_f32 v77, v161, v157
	global_store_dwordx4 v[152:153], v[74:77], off
	v_or_b32_e32 v152, v150, v100
	v_mov_b32_e32 v153, v151
	v_lshl_add_u64 v[152:153], v[152:153], 4, s[56:57]
	v_cvt_pk_bf16_f32 v74, v190, v192
	v_cvt_pk_bf16_f32 v75, v177, v173
	v_cvt_pk_bf16_f32 v76, v169, v163
	v_cvt_pk_bf16_f32 v77, v159, v155
	global_store_dwordx4 v[152:153], v[74:77], off
	v_or_b32_e32 v152, v150, v102
	v_mov_b32_e32 v153, v151
	v_or_b32_e32 v150, v150, v106
	v_cvt_pk_bf16_f32 v74, v165, v193
	v_cvt_pk_bf16_f32 v75, v188, v174
	v_cvt_pk_bf16_f32 v76, v170, v166
	v_cvt_pk_bf16_f32 v77, v160, v156
	v_lshl_add_u64 v[152:153], v[152:153], 4, s[56:57]
	v_lshl_add_u64 v[150:151], v[150:151], 4, s[56:57]
	global_store_dwordx4 v[152:153], v[74:77], off
	s_nop 1
	v_cvt_pk_bf16_f32 v74, v164, v195
	v_cvt_pk_bf16_f32 v75, v191, v176
	v_cvt_pk_bf16_f32 v76, v172, v168
	v_cvt_pk_bf16_f32 v77, v162, v158
	global_store_dwordx4 v[150:151], v[74:77], off
	s_cbranch_vccnz .LBB0_413
	s_lshl_b64 s[66:67], s[40:41], 10
	v_lshl_add_u64 v[74:75], v[86:87], 0, s[66:67]
	global_store_dwordx4 v[74:75], v[78:81], off
